# GEMM K-loop heads and the diff tile loop head aligned to 64 bytes (.p2align 6)
# baseline (speedup 1.0000x reference)
.Lnobar_e1o:
	.p2align	6

.LBB0_586:
	s_add_u32 s8, s62, 0x100
	s_addc_u32 s9, s63, 0
	s_ashr_i32 s47, s46, 31
	s_lshl_b64 s[48:49], s[46:47], 19
	s_add_u32 s52, s85, s48
	s_addc_u32 s53, s93, s49
	s_and_b64 s[48:49], s[44:45], exec
	s_cselect_b32 s47, s53, s35
	s_cselect_b32 s59, s52, s34
	s_ashr_i32 s37, s36, 31
	s_lshl_b64 s[48:49], s[36:37], 19
	s_add_u32 s48, s94, s48
	s_addc_u32 s49, s95, s49
	s_and_b64 s[70:71], s[44:45], exec
	s_cselect_b32 s37, s49, s63
	s_cselect_b32 vcc_lo, s48, s62
	s_add_u32 s62, s34, 0x40080
	s_addc_u32 s63, s35, 0
	v_lshl_add_u64 v[140:141], s[62:63], 0, v[128:129]
	v_lshl_add_u64 v[142:143], s[62:63], 0, v[138:139]
	s_mov_b32 vcc_hi, -2
	s_mov_b64 s[62:63], 0
	.p2align	6

.LBB0_683:
	s_add_u32 s8, s48, 0x100
	s_addc_u32 s9, s49, 0
	s_ashr_i32 s37, s36, 31
	s_lshl_b64 s[44:45], s[36:37], 19
	s_add_u32 s46, s80, s44
	s_addc_u32 s47, s81, s45
	s_and_b64 s[44:45], s[42:43], exec
	s_cselect_b32 s37, s47, s31
	s_cselect_b32 s59, s46, s30
	s_ashr_i32 s35, s34, 31
	s_lshl_b64 s[44:45], s[34:35], 19
	s_add_u32 s44, s82, s44
	s_addc_u32 s45, s83, s45
	s_and_b64 s[52:53], s[42:43], exec
	s_cselect_b32 s35, s45, s49
	s_cselect_b32 s93, s44, s48
	s_add_u32 s48, s30, 0x40080
	s_addc_u32 s49, s31, 0
	v_lshl_add_u64 v[140:141], s[48:49], 0, v[128:129]
	v_lshl_add_u64 v[142:143], s[48:49], 0, v[138:139]
	s_mov_b32 s94, -2
	s_mov_b64 s[48:49], 0
	.p2align	6

.LBB0_1007:
	s_addk_i32 s20, 0x100
	s_add_i32 s10, s10, 1
	s_add_i32 s21, s21, 64
	s_mov_b64 s[6:7], 0x68000
	s_cmp_eq_u32 s19, s20
	v_lshl_add_u64 v[208:209], v[208:209], 0, s[6:7]
	s_waitcnt lgkmcnt(0)
	s_barrier
	s_cbranch_scc1 .LBB0_1024
	.p2align	6

.LBB0_1524:
	s_add_u32 s8, s34, 0x100
	s_addc_u32 s9, s35, 0
	s_add_u32 s34, s26, 0x60080
	s_addc_u32 s35, s27, 0
	v_lshl_add_u64 v[140:141], s[34:35], 0, v[128:129]
	v_lshl_add_u64 v[142:143], s[34:35], 0, v[138:139]
	s_mov_b32 s59, -2
	s_mov_b64 s[34:35], 0
	.p2align	6

.LBB0_1782:
	s_ashr_i32 s23, s22, 31
	s_lshl_b64 s[8:9], s[22:23], 19
	s_add_u32 s24, s34, s8
	s_addc_u32 s25, s35, s9
	s_and_b64 s[8:9], s[38:39], exec
	s_cselect_b32 s8, s25, s7
	s_cselect_b32 s9, s24, s6
	s_ashr_i32 s21, s20, 31
	s_lshl_b64 s[26:27], s[20:21], 19
	s_add_u32 s26, s10, s26
	s_addc_u32 s27, s11, s27
	s_and_b64 s[30:31], s[38:39], exec
	s_cselect_b32 s21, s27, s29
	s_cselect_b32 s23, s26, s28
	s_add_u32 s33, s28, 0x100
	s_addc_u32 s40, s29, 0
	s_add_u32 s6, s6, 0x40080
	v_mov_b32_e32 v2, 0
	s_addc_u32 s7, s7, 0
	s_mov_b32 s41, -2
	v_mov_b32_e32 v3, v2
	v_mov_b32_e32 v4, v2
	v_mov_b32_e32 v5, v2
	v_mov_b32_e32 v6, v2
	v_mov_b32_e32 v7, v2
	v_mov_b32_e32 v8, v2
	v_mov_b32_e32 v9, v2
	v_mov_b32_e32 v14, v2
	v_mov_b32_e32 v15, v2
	v_mov_b32_e32 v16, v2
	v_mov_b32_e32 v17, v2
	v_mov_b32_e32 v22, v2
	v_mov_b32_e32 v23, v2
	v_mov_b32_e32 v24, v2
	v_mov_b32_e32 v25, v2
	v_mov_b32_e32 v30, v2
	v_mov_b32_e32 v31, v2
	v_mov_b32_e32 v32, v2
	v_mov_b32_e32 v33, v2
	v_mov_b32_e32 v38, v2
	v_mov_b32_e32 v39, v2
	v_mov_b32_e32 v40, v2
	v_mov_b32_e32 v41, v2
	v_mov_b32_e32 v46, v2
	v_mov_b32_e32 v47, v2
	v_mov_b32_e32 v48, v2
	v_mov_b32_e32 v49, v2
	v_mov_b32_e32 v54, v2
	v_mov_b32_e32 v55, v2
	v_mov_b32_e32 v56, v2
	v_mov_b32_e32 v57, v2
	v_mov_b32_e32 v10, v2
	v_mov_b32_e32 v11, v2
	v_mov_b32_e32 v12, v2
	v_mov_b32_e32 v13, v2
	v_mov_b32_e32 v18, v2
	v_mov_b32_e32 v19, v2
	v_mov_b32_e32 v20, v2
	v_mov_b32_e32 v21, v2
	v_mov_b32_e32 v26, v2
	v_mov_b32_e32 v27, v2
	v_mov_b32_e32 v28, v2
	v_mov_b32_e32 v29, v2
	v_mov_b32_e32 v34, v2
	v_mov_b32_e32 v35, v2
	v_mov_b32_e32 v36, v2
	v_mov_b32_e32 v37, v2
	v_mov_b32_e32 v42, v2
	v_mov_b32_e32 v43, v2
	v_mov_b32_e32 v44, v2
	v_mov_b32_e32 v45, v2
	v_mov_b32_e32 v50, v2
	v_mov_b32_e32 v51, v2
	v_mov_b32_e32 v52, v2
	v_mov_b32_e32 v53, v2
	v_mov_b32_e32 v58, v2
	v_mov_b32_e32 v59, v2
	v_mov_b32_e32 v60, v2
	v_mov_b32_e32 v61, v2
	v_mov_b32_e32 v62, v2
	v_mov_b32_e32 v63, v2
	v_mov_b32_e32 v64, v2
	v_mov_b32_e32 v65, v2
	v_mov_b32_e32 v66, v2
	v_mov_b32_e32 v67, v2
	v_mov_b32_e32 v68, v2
	v_mov_b32_e32 v69, v2
	v_mov_b32_e32 v70, v2
	v_mov_b32_e32 v71, v2
	v_mov_b32_e32 v72, v2
	v_mov_b32_e32 v73, v2
	v_mov_b32_e32 v78, v2
	v_mov_b32_e32 v79, v2
	v_mov_b32_e32 v80, v2
	v_mov_b32_e32 v81, v2
	v_mov_b32_e32 v86, v2
	v_mov_b32_e32 v87, v2
	v_mov_b32_e32 v88, v2
	v_mov_b32_e32 v89, v2
	v_mov_b32_e32 v94, v2
	v_mov_b32_e32 v95, v2
	v_mov_b32_e32 v96, v2
	v_mov_b32_e32 v97, v2
	v_mov_b32_e32 v102, v2
	v_mov_b32_e32 v103, v2
	v_mov_b32_e32 v104, v2
	v_mov_b32_e32 v105, v2
	v_mov_b32_e32 v110, v2
	v_mov_b32_e32 v111, v2
	v_mov_b32_e32 v112, v2
	v_mov_b32_e32 v113, v2
	v_mov_b32_e32 v118, v2
	v_mov_b32_e32 v119, v2
	v_mov_b32_e32 v120, v2
	v_mov_b32_e32 v121, v2
	v_mov_b32_e32 v74, v2
	v_mov_b32_e32 v75, v2
	v_mov_b32_e32 v76, v2
	v_mov_b32_e32 v77, v2
	v_mov_b32_e32 v82, v2
	v_mov_b32_e32 v83, v2
	v_mov_b32_e32 v84, v2
	v_mov_b32_e32 v85, v2
	v_mov_b32_e32 v90, v2
	v_mov_b32_e32 v91, v2
	v_mov_b32_e32 v92, v2
	v_mov_b32_e32 v93, v2
	v_mov_b32_e32 v98, v2
	v_mov_b32_e32 v99, v2
	v_mov_b32_e32 v100, v2
	v_mov_b32_e32 v101, v2
	v_mov_b32_e32 v106, v2
	v_mov_b32_e32 v107, v2
	v_mov_b32_e32 v108, v2
	v_mov_b32_e32 v109, v2
	v_mov_b32_e32 v114, v2
	v_mov_b32_e32 v115, v2
	v_mov_b32_e32 v116, v2
	v_mov_b32_e32 v117, v2
	v_mov_b32_e32 v122, v2
	v_mov_b32_e32 v123, v2
	v_mov_b32_e32 v124, v2
	v_mov_b32_e32 v125, v2
	v_mov_b32_e32 v126, v2
	v_mov_b32_e32 v127, v2
	v_mov_b32_e32 v128, v2
	v_mov_b32_e32 v129, v2
	s_waitcnt vmcnt(0)
	.p2align	6

.LBB0_1798:
	s_ashr_i32 s17, s16, 31
	s_lshl_b64 s[8:9], s[16:17], 19
	s_add_u32 s20, s30, s8
	s_addc_u32 s21, s31, s9
	s_and_b64 s[8:9], s[18:19], exec
	s_cselect_b32 s8, s21, s27
	s_cselect_b32 s9, s20, s26
	s_ashr_i32 s15, s14, 31
	s_lshl_b64 s[22:23], s[14:15], 19
	s_add_u32 s22, s5, s22
	s_addc_u32 s23, s34, s23
	s_and_b64 s[28:29], s[18:19], exec
	s_cselect_b32 s15, s23, s25
	s_cselect_b32 s17, s22, s24
	s_add_u32 s45, s24, 0x100
	s_addc_u32 s46, s25, 0
	s_add_u32 s24, s26, 0x40080
	v_mov_b32_e32 v2, 0
	s_addc_u32 s25, s27, 0
	s_mov_b32 s47, -2
	v_mov_b32_e32 v3, v2
	v_mov_b32_e32 v4, v2
	v_mov_b32_e32 v5, v2
	v_mov_b32_e32 v6, v2
	v_mov_b32_e32 v7, v2
	v_mov_b32_e32 v8, v2
	v_mov_b32_e32 v9, v2
	v_mov_b32_e32 v10, v2
	v_mov_b32_e32 v11, v2
	v_mov_b32_e32 v12, v2
	v_mov_b32_e32 v13, v2
	v_mov_b32_e32 v18, v2
	v_mov_b32_e32 v19, v2
	v_mov_b32_e32 v20, v2
	v_mov_b32_e32 v21, v2
	v_mov_b32_e32 v26, v2
	v_mov_b32_e32 v27, v2
	v_mov_b32_e32 v28, v2
	v_mov_b32_e32 v29, v2
	v_mov_b32_e32 v34, v2
	v_mov_b32_e32 v35, v2
	v_mov_b32_e32 v36, v2
	v_mov_b32_e32 v37, v2
	v_mov_b32_e32 v42, v2
	v_mov_b32_e32 v43, v2
	v_mov_b32_e32 v44, v2
	v_mov_b32_e32 v45, v2
	v_mov_b32_e32 v50, v2
	v_mov_b32_e32 v51, v2
	v_mov_b32_e32 v52, v2
	v_mov_b32_e32 v53, v2
	v_mov_b32_e32 v14, v2
	v_mov_b32_e32 v15, v2
	v_mov_b32_e32 v16, v2
	v_mov_b32_e32 v17, v2
	v_mov_b32_e32 v22, v2
	v_mov_b32_e32 v23, v2
	v_mov_b32_e32 v24, v2
	v_mov_b32_e32 v25, v2
	v_mov_b32_e32 v30, v2
	v_mov_b32_e32 v31, v2
	v_mov_b32_e32 v32, v2
	v_mov_b32_e32 v33, v2
	v_mov_b32_e32 v38, v2
	v_mov_b32_e32 v39, v2
	v_mov_b32_e32 v40, v2
	v_mov_b32_e32 v41, v2
	v_mov_b32_e32 v46, v2
	v_mov_b32_e32 v47, v2
	v_mov_b32_e32 v48, v2
	v_mov_b32_e32 v49, v2
	v_mov_b32_e32 v54, v2
	v_mov_b32_e32 v55, v2
	v_mov_b32_e32 v56, v2
	v_mov_b32_e32 v57, v2
	v_mov_b32_e32 v58, v2
	v_mov_b32_e32 v59, v2
	v_mov_b32_e32 v60, v2
	v_mov_b32_e32 v61, v2
	v_mov_b32_e32 v62, v2
	v_mov_b32_e32 v63, v2
	v_mov_b32_e32 v64, v2
	v_mov_b32_e32 v65, v2
	v_mov_b32_e32 v66, v2
	v_mov_b32_e32 v67, v2
	v_mov_b32_e32 v68, v2
	v_mov_b32_e32 v69, v2
	v_mov_b32_e32 v70, v2
	v_mov_b32_e32 v71, v2
	v_mov_b32_e32 v72, v2
	v_mov_b32_e32 v73, v2
	v_mov_b32_e32 v74, v2
	v_mov_b32_e32 v75, v2
	v_mov_b32_e32 v76, v2
	v_mov_b32_e32 v77, v2
	v_mov_b32_e32 v82, v2
	v_mov_b32_e32 v83, v2
	v_mov_b32_e32 v84, v2
	v_mov_b32_e32 v85, v2
	v_mov_b32_e32 v90, v2
	v_mov_b32_e32 v91, v2
	v_mov_b32_e32 v92, v2
	v_mov_b32_e32 v93, v2
	v_mov_b32_e32 v98, v2
	v_mov_b32_e32 v99, v2
	v_mov_b32_e32 v100, v2
	v_mov_b32_e32 v101, v2
	v_mov_b32_e32 v106, v2
	v_mov_b32_e32 v107, v2
	v_mov_b32_e32 v108, v2
	v_mov_b32_e32 v109, v2
	v_mov_b32_e32 v114, v2
	v_mov_b32_e32 v115, v2
	v_mov_b32_e32 v116, v2
	v_mov_b32_e32 v117, v2
	v_mov_b32_e32 v78, v2
	v_mov_b32_e32 v79, v2
	v_mov_b32_e32 v80, v2
	v_mov_b32_e32 v81, v2
	v_mov_b32_e32 v86, v2
	v_mov_b32_e32 v87, v2
	v_mov_b32_e32 v88, v2
	v_mov_b32_e32 v89, v2
	v_mov_b32_e32 v94, v2
	v_mov_b32_e32 v95, v2
	v_mov_b32_e32 v96, v2
	v_mov_b32_e32 v97, v2
	v_mov_b32_e32 v102, v2
	v_mov_b32_e32 v103, v2
	v_mov_b32_e32 v104, v2
	v_mov_b32_e32 v105, v2
	v_mov_b32_e32 v110, v2
	v_mov_b32_e32 v111, v2
	v_mov_b32_e32 v112, v2
	v_mov_b32_e32 v113, v2
	v_mov_b32_e32 v118, v2
	v_mov_b32_e32 v119, v2
	v_mov_b32_e32 v120, v2
	v_mov_b32_e32 v121, v2
	v_mov_b32_e32 v122, v2
	v_mov_b32_e32 v123, v2
	v_mov_b32_e32 v124, v2
	v_mov_b32_e32 v125, v2
	v_mov_b32_e32 v126, v2
	v_mov_b32_e32 v127, v2
	v_mov_b32_e32 v128, v2
	v_mov_b32_e32 v129, v2
	.p2align	6

.LBB0_2702:
	s_add_u32 s59, s36, 0x100
	s_addc_u32 s82, s37, 0
	s_ashr_i32 s29, s28, 31
	s_lshl_b64 s[30:31], s[28:29], 21
	s_add_u32 s34, s63, s30
	s_addc_u32 s35, s70, s31
	s_and_b64 s[30:31], s[42:43], exec
	s_cselect_b32 s29, s35, s25
	s_cselect_b32 s83, s34, s24
	s_ashr_i32 s27, s26, 31
	s_lshl_b64 s[30:31], s[26:27], 21
	s_add_u32 s30, s71, s30
	s_addc_u32 s31, s76, s31
	s_and_b64 s[44:45], s[42:43], exec
	s_cselect_b32 s27, s31, s37
	s_cselect_b32 s84, s30, s36
	s_add_u32 s36, s24, 0x100080
	s_addc_u32 s37, s25, 0
	v_lshl_add_u64 v[142:143], s[36:37], 0, v[138:139]
	v_lshl_add_u64 v[144:145], s[36:37], 0, v[140:141]
	s_mov_b32 s85, -2
	s_mov_b64 s[36:37], 0
	.p2align	6

.LBB0_2795:
	s_add_u32 s59, s36, 0x100
	s_addc_u32 s81, s37, 0
	s_ashr_i32 s29, s28, 31
	s_lshl_b64 s[30:31], s[28:29], 21
	s_add_u32 s34, s53, s30
	s_addc_u32 s35, s62, s31
	s_and_b64 s[30:31], s[42:43], exec
	s_cselect_b32 s29, s35, s25
	s_cselect_b32 s82, s34, s24
	s_ashr_i32 s27, s26, 31
	s_lshl_b64 s[30:31], s[26:27], 21
	s_add_u32 s30, s63, s30
	s_addc_u32 s31, s70, s31
	s_and_b64 s[44:45], s[42:43], exec
	s_cselect_b32 s27, s31, s37
	s_cselect_b32 s83, s30, s36
	s_add_u32 s36, s24, 0x100080
	s_addc_u32 s37, s25, 0
	v_lshl_add_u64 v[142:143], s[36:37], 0, v[138:139]
	v_lshl_add_u64 v[144:145], s[36:37], 0, v[140:141]
	s_mov_b32 s84, -2
	s_mov_b64 s[36:37], 0
	.p2align	6

.LBB0_2890:
	s_add_u32 s59, s36, 0x100
	s_addc_u32 s81, s37, 0
	s_ashr_i32 s29, s28, 31
	s_lshl_b64 s[30:31], s[28:29], 21
	s_add_u32 s34, s62, s30
	s_addc_u32 s35, s63, s31
	s_and_b64 s[30:31], s[42:43], exec
	s_cselect_b32 s29, s35, s25
	s_cselect_b32 s82, s34, s24
	s_ashr_i32 s27, s26, 31
	s_lshl_b64 s[30:31], s[26:27], 21
	s_add_u32 s30, s70, s30
	s_addc_u32 s31, s71, s31
	s_and_b64 s[44:45], s[42:43], exec
	s_cselect_b32 s27, s31, s37
	s_cselect_b32 s83, s30, s36
	s_add_u32 s36, s24, 0x100080
	s_addc_u32 s37, s25, 0
	v_lshl_add_u64 v[142:143], s[36:37], 0, v[138:139]
	v_lshl_add_u64 v[144:145], s[36:37], 0, v[140:141]
	s_mov_b32 s84, -2
	s_mov_b64 s[36:37], 0
	.p2align	6

.LBB0_2981:
	s_add_u32 s59, s36, 0x100
	s_addc_u32 s79, s37, 0
	s_ashr_i32 s29, s28, 31
	s_lshl_b64 s[30:31], s[28:29], 21
	s_add_u32 s34, s49, s30
	s_addc_u32 s35, s52, s31
	s_and_b64 s[30:31], s[40:41], exec
	s_cselect_b32 s29, s35, s25
	s_cselect_b32 s80, s34, s24
	s_ashr_i32 s27, s26, 31
	s_lshl_b64 s[30:31], s[26:27], 21
	s_add_u32 s30, s53, s30
	s_addc_u32 s31, s62, s31
	s_and_b64 s[42:43], s[40:41], exec
	s_cselect_b32 s27, s31, s37
	s_cselect_b32 s81, s30, s36
	s_add_u32 s36, s24, 0x100080
	s_addc_u32 s37, s25, 0
	v_lshl_add_u64 v[142:143], s[36:37], 0, v[138:139]
	v_lshl_add_u64 v[144:145], s[36:37], 0, v[140:141]
	s_mov_b32 s82, -2
	s_mov_b64 s[36:37], 0
	.p2align	6
